# diff-attention V tile staged by LDS-DMA (global_load_lds_dwordx4) instead of register slot + ds_write
# speedup vs baseline: 1.0177x; 1.0177x over previous
; template <int LDQ, int LDK, int LDV, int LDO, int DMX> ...
;   const int tid = threadIdx.x, wid = tid >> 6, lane = tid & 63, l16 = lane & 15, g = lane >> 4, rb = wid & 3, ch = wid >> 2;
;   char* V_lds = lds; char* K_lds = lds + D16_OFF_K; float* L_lds = (float*)(lds + D16_OFF_L); float* S_lds = L_lds + 8 * 32;
;   char* P_own = lds + D16_OFF_P + rb * PB_P + ch * 2048 + lane * 16; char* P_oth = lds + D16_OFF_P + rb * PB_P + (1 - ch) * 2048 + lane * 16;
;   constexpr float C = SCALE * 1.4426950408889634f; const float mnC = -mref * C;
;   const int sr = tid >> 4, sc = (tid & 15) * 8;
;   const int vst0 = (sc >> 4) * VP16 + sr * 32 + ((sc >> 3) & 1) * 16, vst1 = vst0 + 1024;
;   const int vlane = (int)(uintptr_t)V_lds + ch * (8 * VP16) + (4 * g + (l16 >> 2)) * 32 + (l16 & 3) * 8;
;   const int kb0 = (32 * ch + l16) * 272 + g * 16;
;   bf16x8 sv0, sv1, sv2, sv3, sk0, sk1;
;   const unsigned koff0 = (unsigned)(sr * LDK + sc) * 2u, koff1 = koff0 + 32u * LDK * 2u, voff0 = (unsigned)(sr * LDV + sc) * 2u, voff1 = voff0 + 32u * LDV * 2u;
; __global__ void __launch_bounds__(NWAVES * 64, 2) __attribute__((amdgpu_num_vgpr(248))) mega_fwd(Args args) {
;     ...
;             const float lam_init = 0.8f - 0.6f * expf(-0.3f);
;             const float d1 = wave_sum(la.in[I_LQ1][lane] * la.in[I_LK1][lane] + la.in[I_LQ1][64 + lane] * la.in[I_LK1][64 + lane]);
;             const float d2 = wave_sum(la.in[I_LQ2][lane] * la.in[I_LK2][lane] + la.in[I_LQ2][64 + lane] * la.in[I_LK2][64 + lane]);
;             const float lam = expf(d1) - expf(d2) + lam_init;
;             for (int it = bid; it < 1024; it += G) { __syncthreads(); const int h = it >> 7, qb = it & 127;
.LBB0_1261:
	s_andn2_saveexec_b64 s[8:9], s[30:31]
	s_cbranch_execz .LBB0_1283
	s_load_dwordx8 s[12:19], s[28:29], 0x90
	s_cmpk_gt_i32 s94, 0x3ff
	s_waitcnt lgkmcnt(0)
	global_load_dword v12, v6, s[12:13]
	global_load_dword v13, v6, s[14:15]
	global_load_dword v14, v6, s[12:13] offset:256
	global_load_dword v15, v6, s[14:15] offset:256
	global_load_dword v16, v6, s[16:17] offset:256
	global_load_dword v17, v6, s[18:19] offset:256
	global_load_dword v18, v6, s[16:17]
	global_load_dword v19, v6, s[18:19]
	s_waitcnt vmcnt(0)
	v_mul_f32_e32 v6, v14, v15
	v_fmac_f32_e32 v6, v12, v13
	v_mul_f32_e32 v14, v16, v17
	ds_bpermute_b32 v12, v8, v6
	v_fmac_f32_e32 v14, v18, v19
	ds_bpermute_b32 v8, v8, v14
	s_waitcnt lgkmcnt(1)
	v_add_f32_e32 v6, v6, v12
	ds_bpermute_b32 v12, v9, v6
	s_waitcnt lgkmcnt(1)
	v_add_f32_e32 v8, v14, v8
	ds_bpermute_b32 v9, v9, v8
	s_waitcnt lgkmcnt(1)
	v_add_f32_e32 v6, v6, v12
	s_waitcnt lgkmcnt(0)
	v_add_f32_e32 v8, v8, v9
	ds_bpermute_b32 v9, v10, v6
	ds_bpermute_b32 v10, v10, v8
	s_waitcnt lgkmcnt(1)
	v_add_f32_e32 v6, v6, v9
	s_waitcnt lgkmcnt(0)
	v_add_f32_e32 v8, v8, v10
	ds_bpermute_b32 v9, v11, v6
	ds_bpermute_b32 v10, v11, v8
	s_waitcnt lgkmcnt(1)
	v_add_f32_e32 v6, v6, v9
	s_waitcnt lgkmcnt(0)
	v_add_f32_e32 v8, v8, v10
	ds_bpermute_b32 v9, v185, v6
	ds_bpermute_b32 v10, v185, v8
	s_waitcnt lgkmcnt(1)
	v_add_f32_e32 v9, v6, v9
	s_waitcnt lgkmcnt(0)
	v_add_f32_e32 v6, v8, v10
	ds_bpermute_b32 v10, v186, v9
	ds_bpermute_b32 v8, v186, v6
	s_cbranch_scc1 .LBB0_1283
	v_lshlrev_b32_e32 v12, 6, v0
	v_lshrrev_b32_e32 v11, 8, v0
	v_and_b32_e32 v12, 0x3000, v12
	s_add_i32 s4, 0, 0x18c00
	v_lshrrev_b32_e32 v189, 4, v2
	v_add_u32_e32 v12, s4, v12
	v_lshlrev_b32_e32 v13, 11, v11
	v_lshlrev_b32_e32 v2, 4, v2
	v_add3_u32 v190, v12, v13, v2
	v_xor_b32_e32 v13, 1, v11
	v_lshlrev_b32_e32 v14, 11, v13
	v_add3_u32 v191, v12, v14, v2
	v_lshrrev_b32_e32 v2, 4, v3
	v_lshlrev_b32_e32 v1, 5, v1
	s_movk_i32 s4, 0x820
	v_and_b32_e32 v188, 15, v0
	v_mad_u32_u24 v1, v2, s4, v1
	s_add_i32 s4, 0, 0x10400
	v_and_or_b32 v1, v5, 16, v1
	v_lshl_or_b32 v5, v11, 5, v188
	s_cmp_lg_u32 0, -1
	v_mul_u32_u24_e32 v5, 0x110, v5
	v_and_b32_e32 v12, 48, v0
	s_cselect_b32 s5, 0, 0
	v_add3_u32 v193, s4, v5, v12
	s_movk_i32 s6, 0x4100
	v_mov_b32_e32 v5, s5
	v_lshlrev_b32_e32 v2, 7, v189
	v_mad_u32_u24 v5, v11, s6, v5
	v_add3_u32 v194, v5, v3, v2
	s_waitcnt lgkmcnt(1)
	v_add_f32_e32 v3, v9, v10
	s_mov_b32 s6, 0x3fb8aa3b
	v_mul_f32_e32 v5, 0x3fb8aa3b, v3
	v_fma_f32 v9, v3, s6, -v5
	v_rndne_f32_e32 v10, v5
	v_fmac_f32_e32 v9, 0x32a5705f, v3
	v_sub_f32_e32 v5, v5, v10
	v_add_f32_e32 v5, v5, v9
	v_exp_f32_e32 v5, v5
	v_cvt_i32_f32_e32 v9, v10
	v_lshlrev_b32_e32 v195, 10, v11
	v_lshlrev_b32_e32 v196, 10, v13
	v_add_u32_e32 v2, 0x8200, v194
	v_add_u32_e32 v197, v2, v195
	v_add_u32_e32 v199, v2, v196
	v_ldexp_f32 v2, v5, v9
	s_waitcnt lgkmcnt(0)
	v_add_f32_e32 v5, v6, v8
	v_mul_f32_e32 v6, 0x3fb8aa3b, v5
	v_fma_f32 v8, v5, s6, -v6
	v_rndne_f32_e32 v9, v6
	v_fmac_f32_e32 v8, 0x32a5705f, v5
	v_sub_f32_e32 v6, v6, v9
	v_add_f32_e32 v6, v6, v8
	v_exp_f32_e32 v6, v6
	v_cvt_i32_f32_e32 v8, v9
	s_mov_b32 s7, 0xc2ce8ed0
	v_cmp_ngt_f32_e32 vcc, s7, v3
	s_mov_b32 s12, 0x42b17218
	v_mov_b32_e32 v9, 0x7f800000
	v_cndmask_b32_e32 v2, 0, v2, vcc
	v_cmp_nlt_f32_e32 vcc, s12, v3
	s_add_u32 s30, s26, 0x42852400
	v_ldexp_f32 v3, v6, v8
	v_cndmask_b32_e32 v2, v9, v2, vcc
	v_cmp_ngt_f32_e32 vcc, s7, v5
	s_load_dwordx2 s[10:11], s[28:29], 0xb0
	s_addc_u32 s31, s27, 0
	v_cndmask_b32_e32 v3, 0, v3, vcc
	v_cmp_nlt_f32_e32 vcc, s12, v5
	s_add_u32 s34, s26, 0x36553400
	v_mov_b32_e32 v159, 0
	v_cndmask_b32_e32 v3, v9, v3, vcc
	v_sub_f32_e32 v2, v2, v3
	s_addc_u32 s35, s27, 0
	v_lshlrev_b32_e32 v4, 1, v4
	v_add_u32_e32 v198, s4, v184
	s_movk_i32 s4, 0xff
	v_add_f32_e32 v160, 0x3eb60549, v2
	s_add_u32 s36, s26, 0x36554400
	v_lshl_add_u32 v4, v188, 4, v4
	v_mov_b32_e32 v5, v159
	v_lshrrev_b32_e32 v187, 6, v0
	s_movk_i32 s28, 0x3000
	v_add_u32_e32 v1, 0, v1
	s_mov_b32 s29, 0x60000
	v_add_u32_e32 v158, 0x60000, v156
	v_cmp_lt_u32_e64 s[4:5], s4, v0
	s_addc_u32 s37, s27, 0
	v_mul_f32_e32 v200, 0xbe0293ee, v7
	v_mov_b32_e32 v161, v160
	v_mov_b32_e32 v2, v160
	v_mov_b32_e32 v3, v160
	v_and_b32_e32 v253, 63, v0
	v_lshrrev_b32_e32 v252, 1, v253
	v_mul_u32_u24_e32 v252, 0x3000, v252
	v_and_b32_e32 v253, 1, v253
	v_lshl_add_u32 v252, v253, 4, v252
	v_lshrrev_b32_e32 v253, 6, v0
	v_lshl_add_u32 v253, v253, 6, v252
	v_lshrrev_b32_e32 v252, 6, v0
	v_mul_u32_u24_e32 v252, 0x1040, v252
	s_nop 0
	v_readfirstlane_b32 s84, v252
	v_lshl_add_u64 v[162:163], s[26:27], 0, v[4:5]
	s_mov_b32 s26, 0x30000
	s_mov_b32 s27, 0xc0000
	s_mov_b32 s38, 0x120000
	s_mov_b32 s39, 0x180000
	s_mov_b32 s40, 0x1e0000
	s_mov_b32 s41, 0x36793000
	s_mov_b32 s42, 0x367f3000
	s_mov_b32 s43, 0x366d4000
	s_mov_b32 s44, 0x36734000
	s_add_i32 s45, 0, 0x20c00
	s_mov_b64 s[12:13], 0x40000
	s_add_i32 s46, 0, 0x21000
	v_mov_b32_e32 v201, 0x358637bd
	s_mov_b32 s47, 0xf800000
	v_mov_b32_e32 v202, 0x260
	s_mov_b32 s48, 0x3f24fd5c
	s_movk_i32 s49, 0x7fff
	s_mov_b64 s[14:15], 0x10000
	v_mov_b32_e32 v203, 1
	s_mov_b32 s50, s94
	s_branch .LBB0_1265

; template <int LDQ, int LDK, int LDV, int LDO, int DMX> ...
;     ...
;   const bf16* Kh = Kh0 + pass * 128;
;   float ls0 = 0.f, ls1 = 0.f; f32x4a o[8][2] = {}; bf16x8 qr[2][4]; f32x4a s[2][2]; bf16x8 po[2];
;   { int l16q = l16, gq = g, widq = wid; asm volatile("" : "+v"(l16q), "+v"(gq), "+v"(widq));
;     const bf16* Qw = Qb0 + pass * 128 + (long)((widq & 3) * QBLK + l16q) * LDQ + gq * 8;
; #pragma unroll
;     for (int qt = 0; qt < 2; ++qt)
; #pragma unroll
;       for (int ds = 0; ds < 4; ++ds) qr[qt][ds] = *reinterpret_cast<const bf16x8*>(Qw + (long)qt * 16 * LDQ + ds * 32); }
; __global__ void __launch_bounds__(NWAVES * 64, 2) __attribute__((amdgpu_num_vgpr(248))) mega_fwd(Args args) {
;     ...
;             for (int it = bid; it < 1024; it += G) { __syncthreads(); const int h = it >> 7, qb = it & 127;
;                 att::attn_diff16_body<OD_LD, OD_LD, OD_LD, 4096, DM>(PROJ + (size_t)qb * 128 * OD_LD + h * 256, PROJ + 2048 + h * 256, PROJ + 4096 + h * 256,
;                                                                 O1 + (size_t)qb * 128 * 4096 + h * 512, MIX + (size_t)qb * 128 * DM + h * 256, NTOK, (char*)lds_raw, mraw, lam, 1.0f - lam_init, la.in[I_ODSG]); } }
.LBB0_1265:
	s_lshl_b32 s6, s50, 7
	s_and_b32 s18, s6, 0x3f80
	s_ashr_i32 s16, s50, 7
	s_mul_i32 s6, s18, 0x3000
	s_add_u32 s17, s1, s6
	s_addc_u32 s19, s2, 0
	s_lshl_b32 s6, s16, 8
	s_ashr_i32 s7, s6, 31
	s_lshl_b64 s[6:7], s[6:7], 1
	s_add_u32 s51, s17, s6
	s_addc_u32 s52, s19, s7
	s_add_u32 s53, s34, s6
	s_addc_u32 s54, s35, s7
	s_add_u32 s20, s36, s6
	s_addc_u32 s21, s37, s7
	s_mov_b64 s[72:73], s[20:21]
	s_lshl_b32 s17, s18, 14
	s_add_u32 s19, s3, s17
	s_addc_u32 s22, s33, 0
	s_lshl_b32 s16, s16, 9
	s_ashr_i32 s17, s16, 31
	s_lshl_b64 s[16:17], s[16:17], 2
	s_add_u32 s16, s19, s16
	s_addc_u32 s17, s22, s17
	s_lshl_b32 s18, s18, 12
	s_add_u32 s18, s30, s18
	s_addc_u32 s19, s31, 0
	s_add_u32 s18, s18, s6
	s_addc_u32 s19, s19, s7
	v_lshl_add_u64 v[164:165], s[20:21], 0, v[156:157]
	v_lshl_add_u64 v[166:167], s[20:21], 0, v[158:159]
	s_add_u32 s20, s20, 0xc0000
	s_addc_u32 s21, s21, 0
	v_lshl_add_u64 v[168:169], s[20:21], 0, v[156:157]
	v_lshl_add_u64 v[170:171], s[20:21], 0, v[158:159]
	v_lshl_add_u64 v[172:173], v[162:163], 0, s[6:7]
	s_mov_b64 s[6:7], 0
	s_mov_b64 s[20:21], -1
	s_waitcnt lgkmcnt(0)
	s_barrier
	s_branch .LBB0_1267

; #define ELOADV(kt) do { const char* vb_ = (const char*)Vh + (size_t)(kt) * (64 * LDV * 2); sv0 = *(const bf16x8*)(vb_ + voff0); sv1 = *(const bf16x8*)(vb_ + voff1); sv2 = *(const bf16x8*)(vb_ + voff0 + 256); sv3 = *(const bf16x8*)(vb_ + voff1 + 256); } while (0)
; #define ELOADK(kt) do { const char* kb_ = (const char*)Kh + (size_t)(kt) * (64 * LDK * 2); sk0 = *(const bf16x8*)(kb_ + koff0); sk1 = *(const bf16x8*)(kb_ + koff1); } while (0)
; #define EWRITEV(b) do { char* d_ = V_lds + (b) * D16_V; *(bf16x8*)(d_ + vst0) = sv0; *(bf16x8*)(d_ + vst1) = sv1; *(bf16x8*)(d_ + 8 * VP16 + vst0) = sv2; *(bf16x8*)(d_ + 8 * VP16 + vst1) = sv3; } while (0)
; #define EWRITEK(b) do { char* d_ = K_lds + (b) * PB_K; *(bf16x8*)(d_ + KSWZ(sr, sc * 2)) = sk0; *(bf16x8*)(d_ + KSWZ(32 + sr, sc * 2)) = sk1; } while (0)
; template <int LDQ, int LDK, int LDV, int LDO, int DMX> ...
;     ...
;   { int l16q = l16, gq = g, widq = wid; asm volatile("" : "+v"(l16q), "+v"(gq), "+v"(widq));
;     const bf16* Qw = Qb0 + pass * 128 + (long)((widq & 3) * QBLK + l16q) * LDQ + gq * 8;
; #pragma unroll
;     for (int qt = 0; qt < 2; ++qt)
; #pragma unroll
;       for (int ds = 0; ds < 4; ++ds) qr[qt][ds] = *reinterpret_cast<const bf16x8*>(Qw + (long)qt * 16 * LDQ + ds * 32); }
;   ELOADK(0); ELOADV(0); asm volatile("s_waitcnt vmcnt(0)" ::: "memory"); EWRITEK(0); EWRITEV(0);
;   ELOADK(1); asm volatile("s_waitcnt vmcnt(0)" ::: "memory"); EWRITEK(1); __syncthreads();
;   ELOADK(2); ELOADV(1);
;   EQK(0); ESM(0);
;   if (wid >= 4) __builtin_amdgcn_s_setprio(1);
.LBB0_1267:
	v_mov_b32_e32 v6, v189
	v_mov_b32_e32 v4, v188
	v_mov_b32_e32 v5, v187
	s_lshl_b64 s[22:23], s[6:7], 1
	s_add_u32 s56, s51, s22
	v_lshlrev_b32_e32 v5, 5, v5
	s_addc_u32 s57, s52, s23
	v_and_b32_e32 v5, 0x60, v5
	v_add_u32_e32 v7, v5, v4
	v_mov_b64_e32 v[4:5], s[56:57]
	v_lshlrev_b32_e32 v6, 3, v6
	v_mad_i64_i32 v[4:5], s[56:57], v7, s28, v[4:5]
	v_ashrrev_i32_e32 v7, 31, v6
	v_lshl_add_u64 v[20:21], v[6:7], 1, v[4:5]
	s_add_u32 s22, s53, s22
	v_add_co_u32_e32 v32, vcc, s26, v20
	s_addc_u32 s23, s54, s23
	s_nop 0
	v_addc_co_u32_e32 v33, vcc, 0, v21, vcc
	v_lshl_add_u64 v[76:77], s[22:23], 0, v[156:157]
	v_add_co_u32_e32 v40, vcc, s29, v76
	global_load_dwordx4 v[4:7], v[20:21], off
	global_load_dwordx4 v[8:11], v[20:21], off offset:64
	global_load_dwordx4 v[12:15], v[20:21], off offset:128
	global_load_dwordx4 v[16:19], v[20:21], off offset:192
	v_addc_co_u32_e32 v41, vcc, 0, v77, vcc
	v_add_co_u32_e32 v60, vcc, s27, v76
	global_load_dwordx4 v[20:23], v[32:33], off
	global_load_dwordx4 v[24:27], v[32:33], off offset:64
	global_load_dwordx4 v[28:31], v[32:33], off offset:128
	s_nop 0
	global_load_dwordx4 v[32:35], v[32:33], off offset:192
	v_addc_co_u32_e32 v61, vcc, 0, v77, vcc
	v_add_co_u32_e32 v64, vcc, s38, v76
	global_load_dwordx4 v[36:39], v[76:77], off
	s_nop 0
	global_load_dwordx4 v[40:43], v[40:41], off
	s_nop 0
	global_load_dwordx4 v[44:47], v[164:165], off
	global_load_dwordx4 v[48:51], v[164:165], off offset:256
	global_load_dwordx4 v[52:55], v[166:167], off
	global_load_dwordx4 v[56:59], v[166:167], off offset:256
	s_waitcnt vmcnt(0)
	v_addc_co_u32_e32 v65, vcc, 0, v77, vcc
	global_load_dwordx4 v[60:63], v[60:61], off
	s_nop 0
	global_load_dwordx4 v[64:67], v[64:65], off
	v_add_u32_e32 v68, 0, v184
	v_add_u32_e32 v69, 0x10400, v68
	v_add_u32_e32 v68, 0x14800, v68
	s_waitcnt vmcnt(0)
	ds_write_b128 v69, v[36:39]
	s_waitcnt vmcnt(6)
	ds_write_b128 v69, v[40:43] offset:8704
	s_waitcnt vmcnt(5)
	ds_write_b128 v1, v[44:47]
	s_waitcnt vmcnt(3)
	ds_write_b128 v1, v[52:55] offset:1024
	ds_write_b128 v1, v[48:51] offset:16640
	s_waitcnt vmcnt(2)
	ds_write_b128 v1, v[56:59] offset:17664
	s_waitcnt vmcnt(0)
	s_waitcnt vmcnt(1)
	ds_write_b128 v68, v[60:63]
	s_waitcnt vmcnt(0)
	ds_write_b128 v68, v[64:67] offset:8704
	s_waitcnt lgkmcnt(0)
	s_barrier
	ds_read_b128 v[36:39], v193
	ds_read_b128 v[40:43], v193 offset:64
	ds_read_b128 v[48:51], v193 offset:4352
	ds_read_b128 v[52:55], v193 offset:4416
	s_waitcnt lgkmcnt(3)
	v_mfma_f32_16x16x32_bf16 v[44:47], v[36:39], v[4:7], 0
	v_mfma_f32_16x16x32_bf16 v[36:39], v[36:39], v[20:23], 0
	s_waitcnt lgkmcnt(1)
	v_mfma_f32_16x16x32_bf16 v[56:59], v[48:51], v[4:7], 0
	v_mfma_f32_16x16x32_bf16 v[48:51], v[48:51], v[20:23], 0
	v_mfma_f32_16x16x32_bf16 v[44:47], v[40:43], v[8:11], v[44:47]
	v_mfma_f32_16x16x32_bf16 v[36:39], v[40:43], v[24:27], v[36:39]
	s_waitcnt lgkmcnt(0)
	v_mfma_f32_16x16x32_bf16 v[40:43], v[52:55], v[8:11], v[56:59]
	v_mfma_f32_16x16x32_bf16 v[48:51], v[52:55], v[24:27], v[48:51]
	ds_read_b128 v[52:55], v193 offset:128
	s_nop 0
	ds_read_b128 v[56:59], v193 offset:192
	s_waitcnt lgkmcnt(1)
	v_mfma_f32_16x16x32_bf16 v[44:47], v[52:55], v[12:15], v[44:47]
	v_mfma_f32_16x16x32_bf16 v[36:39], v[52:55], v[28:31], v[36:39]
	ds_read_b128 v[52:55], v193 offset:4480
	ds_read_b128 v[60:63], v193 offset:4544
	s_waitcnt lgkmcnt(1)
	v_mfma_f32_16x16x32_bf16 v[64:67], v[52:55], v[12:15], v[40:43]
	s_nop 2
	v_add_co_u32_e32 v40, vcc, s39, v76
	v_mfma_f32_16x16x32_bf16 v[68:71], v[52:55], v[28:31], v[48:51]
	s_nop 0
	v_addc_co_u32_e32 v41, vcc, 0, v77, vcc
	v_add_co_u32_e32 v42, vcc, s40, v76
	v_mfma_f32_16x16x32_bf16 v[72:75], v[56:59], v[16:19], v[44:47]
	s_nop 0
	v_addc_co_u32_e32 v43, vcc, 0, v77, vcc
	v_mfma_f32_16x16x32_bf16 v[76:79], v[56:59], v[32:35], v[36:39]
	global_load_dwordx4 v[52:55], v[40:41], off
	global_load_dwordx4 v[56:59], v[42:43], off
	s_nop 0
	s_waitcnt lgkmcnt(0)
	v_mfma_f32_16x16x32_bf16 v[64:67], v[60:63], v[16:19], v[64:67]
	v_mfma_f32_16x16x32_bf16 v[68:71], v[60:63], v[32:35], v[68:71]
	v_fmamk_f32 v61, v73, 0x3e0293ee, v200
	v_exp_f32_e32 v62, v61
	v_fmamk_f32 v61, v74, 0x3e0293ee, v200
	v_fmamk_f32 v60, v72, 0x3e0293ee, v200
	v_exp_f32_e32 v72, v61
	v_fmamk_f32 v61, v75, 0x3e0293ee, v200
	s_nop 0
	v_fmamk_f32 v64, v64, 0x3e0293ee, v200
	v_exp_f32_e32 v74, v61
	v_fmamk_f32 v61, v76, 0x3e0293ee, v200
	v_exp_f32_e32 v76, v64
	v_fmamk_f32 v64, v65, 0x3e0293ee, v200
	v_fmamk_f32 v73, v78, 0x3e0293ee, v200
	v_exp_f32_e32 v78, v64
	v_fmamk_f32 v64, v66, 0x3e0293ee, v200
	v_exp_f32_e32 v80, v64
	v_fmamk_f32 v64, v67, 0x3e0293ee, v200
	v_exp_f32_e32 v82, v64
	v_fmamk_f32 v64, v68, 0x3e0293ee, v200
	v_fmamk_f32 v63, v77, 0x3e0293ee, v200
	v_exp_f32_e32 v77, v64
	v_fmamk_f32 v64, v69, 0x3e0293ee, v200
	v_fmamk_f32 v75, v79, 0x3e0293ee, v200
	v_exp_f32_e32 v79, v64
	v_fmamk_f32 v64, v70, 0x3e0293ee, v200
	v_exp_f32_e32 v81, v64
	v_fmamk_f32 v64, v71, 0x3e0293ee, v200
	v_exp_f32_e32 v60, v60
	v_exp_f32_e32 v61, v61
	v_exp_f32_e32 v63, v63
	v_exp_f32_e32 v73, v73
	v_exp_f32_e32 v75, v75
	v_exp_f32_e32 v83, v64
	v_cvt_pk_bf16_f32 v64, v60, v62
	v_cvt_pk_bf16_f32 v65, v72, v74
	v_cvt_pk_bf16_f32 v66, v76, v78
	v_cvt_pk_bf16_f32 v67, v80, v82
	v_cvt_pk_bf16_f32 v68, v61, v63
	v_cvt_pk_bf16_f32 v69, v73, v75
	v_cvt_pk_bf16_f32 v70, v77, v79
	v_cvt_pk_bf16_f32 v71, v81, v83
	ds_write_b128 v190, v[64:67]
	ds_write_b128 v190, v[68:71] offset:1024
	s_and_saveexec_b64 s[22:23], s[4:5]
	s_setprio 1
	s_or_b64 exec, exec, s[22:23]
	v_pk_add_f32 v[60:61], v[60:61], v[62:63]
	v_pk_add_f32 v[62:63], v[72:73], v[74:75]
	v_pk_add_f32 v[72:73], v[80:81], v[82:83]
; #define SBAR() __builtin_amdgcn_sched_barrier(0)
; #define ELOADV(kt) do { const char* vb_ = (const char*)Vh + (size_t)(kt) * (64 * LDV * 2); sv0 = *(const bf16x8*)(vb_ + voff0); sv1 = *(const bf16x8*)(vb_ + voff1); sv2 = *(const bf16x8*)(vb_ + voff0 + 256); sv3 = *(const bf16x8*)(vb_ + voff1 + 256); } while (0)
; #define ELOADK(kt) do { const char* kb_ = (const char*)Kh + (size_t)(kt) * (64 * LDK * 2); sk0 = *(const bf16x8*)(kb_ + koff0); sk1 = *(const bf16x8*)(kb_ + koff1); } while (0)
; #define EWRITEV(b) do { char* d_ = V_lds + (b) * D16_V; *(bf16x8*)(d_ + vst0) = sv0; *(bf16x8*)(d_ + vst1) = sv1; *(bf16x8*)(d_ + 8 * VP16 + vst0) = sv2; *(bf16x8*)(d_ + 8 * VP16 + vst1) = sv3; } while (0)
; #define EWRITEK(b) do { char* d_ = K_lds + (b) * PB_K; *(bf16x8*)(d_ + KSWZ(sr, sc * 2)) = sk0; *(bf16x8*)(d_ + KSWZ(32 + sr, sc * 2)) = sk1; } while (0)
; template <int LDQ, int LDK, int LDV, int LDO, int DMX> ...
;     ...
;   for (int t = 0; t < NT; ++t) {
;     __syncthreads();
;     bf16x8 pp[2]; { const char* d_ = P_oth + (t & 1) * (4 * PB_P); pp[0] = *(const bf16x8*)(d_); pp[1] = *(const bf16x8*)(d_ + 1024); }
;     const bf16x8 pc[2] = {po[0], po[1]};
;     const bool more = t + 1 < NT;
;     if (more) EQK((t + 1) & 1);
;     const int vb = vlane + (t & 1) * (int)D16_V, vbo = vb + ch * 1024, vbp = vb + (1 - ch) * 1024;
;     SBAR(); pv16d<0>(o, vbo, vbp, pc, pp); SBAR();
;     asm volatile("s_waitcnt vmcnt(0)" ::: "memory");
;     if (t + 2 < NT) EWRITEK(t & 1);
;     if (t + 1 < NT) EWRITEV((t + 1) & 1);
;     ELOADK(t + 3); ELOADV(t + 2);
;     SBAR(); pv16d<4>(o, vbo, vbp, pc, pp); SBAR();
;     if (more) ESM((t + 1) & 1);
	v_pk_add_f32 v[60:61], v[60:61], v[62:63]
	v_pk_add_f32 v[62:63], v[76:77], v[78:79]
	v_mov_b32_e32 v112, 0
	v_pk_add_f32 v[62:63], v[62:63], v[72:73]
	s_xor_b64 s[20:21], s[20:21], -1
	v_pk_add_f32 v[60:61], v[60:61], v[62:63]
	s_mov_b32 s55, 1
	v_pk_add_f32 v[174:175], v[60:61], 0 op_sel_hi:[1,0]
	s_add_u32 s74, s72, 0xc0000
	s_addc_u32 s75, s73, 0
	s_add_u32 s76, s74, 0x60000
	s_addc_u32 s77, s75, 0
	v_lshl_add_u64 v[176:177], s[6:7], 1, v[172:173]
	s_mov_b64 s[6:7], 0
	s_movk_i32 s56, 0x4000
	v_mov_b32_e32 v113, v112
	v_mov_b32_e32 v114, v112
	v_mov_b32_e32 v115, v112
	v_mov_b32_e32 v120, v112
	v_mov_b32_e32 v121, v112
	v_mov_b32_e32 v122, v112
	v_mov_b32_e32 v123, v112
	v_mov_b32_e32 v124, v112
	v_mov_b32_e32 v125, v112
	v_mov_b32_e32 v126, v112
	v_mov_b32_e32 v127, v112
	v_mov_b32_e32 v128, v112
	v_mov_b32_e32 v129, v112
	v_mov_b32_e32 v130, v112
	v_mov_b32_e32 v131, v112
	v_mov_b32_e32 v108, v112
	v_mov_b32_e32 v109, v112
	v_mov_b32_e32 v110, v112
	v_mov_b32_e32 v111, v112
	v_mov_b32_e32 v116, v112
	v_mov_b32_e32 v117, v112
	v_mov_b32_e32 v118, v112
	v_mov_b32_e32 v119, v112
	v_mov_b32_e32 v100, v112
	v_mov_b32_e32 v101, v112
	v_mov_b32_e32 v102, v112
	v_mov_b32_e32 v103, v112
	v_mov_b32_e32 v104, v112
	v_mov_b32_e32 v105, v112
	v_mov_b32_e32 v106, v112
	v_mov_b32_e32 v107, v112
	v_mov_b32_e32 v84, v112
	v_mov_b32_e32 v85, v112
	v_mov_b32_e32 v86, v112
	v_mov_b32_e32 v87, v112
	v_mov_b32_e32 v92, v112
	v_mov_b32_e32 v93, v112
	v_mov_b32_e32 v94, v112
	v_mov_b32_e32 v95, v112
	v_mov_b32_e32 v88, v112
	v_mov_b32_e32 v89, v112
	v_mov_b32_e32 v90, v112
	v_mov_b32_e32 v91, v112
	v_mov_b32_e32 v96, v112
	v_mov_b32_e32 v97, v112
	v_mov_b32_e32 v98, v112
	v_mov_b32_e32 v99, v112
	v_mov_b32_e32 v60, v112
	v_mov_b32_e32 v61, v112
	v_mov_b32_e32 v62, v112
	v_mov_b32_e32 v63, v112
	v_mov_b32_e32 v80, v112
	v_mov_b32_e32 v81, v112
	v_mov_b32_e32 v82, v112
	v_mov_b32_e32 v83, v112
	v_mov_b32_e32 v72, v112
	v_mov_b32_e32 v73, v112
	v_mov_b32_e32 v74, v112
	v_mov_b32_e32 v75, v112
	v_mov_b32_e32 v76, v112
	v_mov_b32_e32 v77, v112
	v_mov_b32_e32 v78, v112
	v_mov_b32_e32 v79, v112
	s_branch .LBB0_1271
.LBB0_1271:
	s_add_i32 s60, s55, -1
	s_and_b32 s57, s60, 1
	s_bitcmp1_b32 s55, 0
	s_cselect_b64 s[22:23], -1, 0
	s_and_b64 s[58:59], s[22:23], exec
	s_cselect_b32 s58, 0x4400, 0
	s_cselect_b32 s85, 0x8200, 0
	s_add_i32 s85, s85, s84
	v_add_u32_e32 v178, s58, v193
	s_waitcnt vmcnt(2) lgkmcnt(0)
	s_barrier
	ds_read_b128 v[132:135], v178
	ds_read_b128 v[136:139], v178 offset:64
	ds_read_b128 v[144:147], v178 offset:4352
	ds_read_b128 v[148:151], v178 offset:4416
	s_mov_b32 m0, s85
	s_nop 0
	global_load_lds_dwordx4 v253, s[74:75]
	s_add_i32 m0, s85, 0x800
	s_nop 0
	global_load_lds_dwordx4 v253, s[74:75] offset:32
	s_add_i32 m0, s85, 0x400
	s_nop 0
	global_load_lds_dwordx4 v253, s[76:77]
	s_add_i32 m0, s85, 0xc00
	s_nop 0
	global_load_lds_dwordx4 v253, s[76:77] offset:32
	s_add_u32 s74, s74, 0xc0000
	s_addc_u32 s75, s75, 0
	s_add_u32 s76, s76, 0xc0000
	s_addc_u32 s77, s77, 0
	s_waitcnt lgkmcnt(3)
	v_mfma_f32_16x16x32_bf16 v[140:143], v[132:135], v[4:7], 0
	s_mul_i32 s58, s57, 0x8200
	v_mfma_f32_16x16x32_bf16 v[132:135], v[132:135], v[20:23], 0
	s_waitcnt lgkmcnt(1)
	v_mfma_f32_16x16x32_bf16 v[152:155], v[144:147], v[4:7], 0
	v_mfma_f32_16x16x32_bf16 v[144:147], v[144:147], v[20:23], 0
	v_mfma_f32_16x16x32_bf16 v[140:143], v[136:139], v[8:11], v[140:143]
	v_mfma_f32_16x16x32_bf16 v[132:135], v[136:139], v[24:27], v[132:135]
	s_waitcnt lgkmcnt(0)
	v_mfma_f32_16x16x32_bf16 v[136:139], v[148:151], v[8:11], v[152:155]
	v_mfma_f32_16x16x32_bf16 v[144:147], v[148:151], v[24:27], v[144:147]
	ds_read_b128 v[148:151], v178 offset:128
	s_nop 0
	ds_read_b128 v[152:155], v178 offset:192
	s_waitcnt lgkmcnt(1)
	v_mfma_f32_16x16x32_bf16 v[140:143], v[148:151], v[12:15], v[140:143]
	v_mfma_f32_16x16x32_bf16 v[132:135], v[148:151], v[28:31], v[132:135]
	ds_read_b128 v[148:151], v178 offset:4480
	ds_read_b128 v[180:183], v178 offset:4544
	s_waitcnt lgkmcnt(1)
	v_mfma_f32_16x16x32_bf16 v[136:139], v[148:151], v[12:15], v[136:139]
	v_mfma_f32_16x16x32_bf16 v[204:207], v[148:151], v[28:31], v[144:147]
	v_mfma_f32_16x16x32_bf16 v[144:147], v[152:155], v[16:19], v[140:143]
	v_mfma_f32_16x16x32_bf16 v[140:143], v[152:155], v[32:35], v[132:135]
	s_nop 2
	v_lshl_add_u32 v132, s57, 14, v191
	ds_read_b128 v[148:151], v132
	ds_read_b128 v[152:155], v132 offset:1024
	v_add_u32_e32 v132, s58, v194
	s_waitcnt lgkmcnt(2)
	v_mfma_f32_16x16x32_bf16 v[136:139], v[180:183], v[16:19], v[136:139]
	v_add_u32_e32 v179, v132, v195
	v_add_u32_e32 v178, v132, v196
	v_mfma_f32_16x16x32_bf16 v[132:135], v[180:183], v[32:35], v[204:207]
	ds_read_b64_tr_b16 v[180:181], v179 offset:0
	ds_read_b64_tr_b16 v[182:183], v179 offset:0x200
	ds_read_b64_tr_b16 v[204:205], v178 offset:0
	ds_read_b64_tr_b16 v[206:207], v178 offset:0x200
	ds_read_b64_tr_b16 v[208:209], v179 offset:0x820
	ds_read_b64_tr_b16 v[210:211], v179 offset:0xa20
	ds_read_b64_tr_b16 v[212:213], v178 offset:0x820
	ds_read_b64_tr_b16 v[214:215], v178 offset:0xa20
	ds_read_b64_tr_b16 v[216:217], v179 offset:0x1040
	ds_read_b64_tr_b16 v[218:219], v179 offset:0x1240
	ds_read_b64_tr_b16 v[220:221], v178 offset:0x1040
	ds_read_b64_tr_b16 v[222:223], v178 offset:0x1240
	s_waitcnt lgkmcnt(4)
	s_nop 0
	v_mfma_f32_16x16x32_bf16 v[128:131], v[180:183], v[64:67], v[128:131]
	v_mfma_f32_16x16x32_bf16 v[124:127], v[180:183], v[68:71], v[124:127]
	v_mfma_f32_16x16x32_bf16 v[120:123], v[208:211], v[64:67], v[120:123]
	v_mfma_f32_16x16x32_bf16 v[112:115], v[208:211], v[68:71], v[112:115]
	s_waitcnt lgkmcnt(1)
	v_mfma_f32_16x16x32_bf16 v[128:131], v[204:207], v[148:151], v[128:131]
	s_waitcnt lgkmcnt(0)
	v_mfma_f32_16x16x32_bf16 v[124:127], v[204:207], v[152:155], v[124:127]
	v_mfma_f32_16x16x32_bf16 v[120:123], v[212:215], v[148:151], v[120:123]
	v_mfma_f32_16x16x32_bf16 v[112:115], v[212:215], v[152:155], v[112:115]
	ds_read_b64_tr_b16 v[180:181], v179 offset:0x1860
	ds_read_b64_tr_b16 v[182:183], v179 offset:0x1a60
	ds_read_b64_tr_b16 v[204:205], v178 offset:0x1860
	ds_read_b64_tr_b16 v[206:207], v178 offset:0x1a60
	s_waitcnt lgkmcnt(4)
	v_mfma_f32_16x16x32_bf16 v[108:111], v[216:219], v[64:67], v[108:111]
	s_waitcnt lgkmcnt(0)
	v_mfma_f32_16x16x32_bf16 v[116:119], v[216:219], v[68:71], v[116:119]
	v_mfma_f32_16x16x32_bf16 v[108:111], v[220:223], v[148:151], v[108:111]
	v_mfma_f32_16x16x32_bf16 v[116:119], v[220:223], v[152:155], v[116:119]
	v_mfma_f32_16x16x32_bf16 v[100:103], v[180:183], v[64:67], v[100:103]
	v_mfma_f32_16x16x32_bf16 v[104:107], v[180:183], v[68:71], v[104:107]
	v_mfma_f32_16x16x32_bf16 v[100:103], v[204:207], v[148:151], v[100:103]
	v_mfma_f32_16x16x32_bf16 v[104:107], v[204:207], v[152:155], v[104:107]
	s_waitcnt vmcnt(4)
	s_cmpk_gt_u32 s60, 0x101
	s_cbranch_scc1 .Lvd_kskip
	s_mulk_i32 s57, 0x4400
	v_add_u32_e32 v180, s57, v198
	s_nop 0
	ds_write_b128 v180, v[52:55]
	ds_write_b128 v180, v[56:59] offset:8704
; #define SBAR() __builtin_amdgcn_sched_barrier(0)
; #define ELOADV(kt) do { const char* vb_ = (const char*)Vh + (size_t)(kt) * (64 * LDV * 2); sv0 = *(const bf16x8*)(vb_ + voff0); sv1 = *(const bf16x8*)(vb_ + voff1); sv2 = *(const bf16x8*)(vb_ + voff0 + 256); sv3 = *(const bf16x8*)(vb_ + voff1 + 256); } while (0)
; #define ELOADK(kt) do { const char* kb_ = (const char*)Kh + (size_t)(kt) * (64 * LDK * 2); sk0 = *(const bf16x8*)(kb_ + koff0); sk1 = *(const bf16x8*)(kb_ + koff1); } while (0)
; #define EWRITEV(b) do { char* d_ = V_lds + (b) * D16_V; *(bf16x8*)(d_ + vst0) = sv0; *(bf16x8*)(d_ + vst1) = sv1; *(bf16x8*)(d_ + 8 * VP16 + vst0) = sv2; *(bf16x8*)(d_ + 8 * VP16 + vst1) = sv3; } while (0)
; #define EWRITEK(b) do { char* d_ = K_lds + (b) * PB_K; *(bf16x8*)(d_ + KSWZ(sr, sc * 2)) = sk0; *(bf16x8*)(d_ + KSWZ(32 + sr, sc * 2)) = sk1; } while (0)
; template <int LDQ, int LDK, int LDV, int LDO, int DMX> ...
;     ...
;     asm volatile("s_waitcnt vmcnt(0)" ::: "memory");
;     if (t + 2 < NT) EWRITEK(t & 1);
;     if (t + 1 < NT) EWRITEV((t + 1) & 1);
;     ELOADK(t + 3); ELOADV(t + 2);
;     SBAR(); pv16d<4>(o, vbo, vbp, pc, pp); SBAR();
;     if (more) ESM((t + 1) & 1);
;   }
.Lvd_kskip:
	v_lshl_add_u64 v[36:37], v[176:177], 0, s[6:7]
	v_add_co_u32_e32 v38, vcc, s41, v36
	s_nop 1
	v_addc_co_u32_e32 v39, vcc, 0, v37, vcc
	v_add_co_u32_e32 v36, vcc, s42, v36
	s_nop 1
	v_addc_co_u32_e32 v37, vcc, 0, v37, vcc
	global_load_dwordx4 v[52:55], v[38:39], off offset:1024
	global_load_dwordx4 v[56:59], v[36:37], off offset:1024
	ds_read_b64_tr_b16 v[180:181], v179 offset:0x2080
	ds_read_b64_tr_b16 v[182:183], v179 offset:0x2280
	ds_read_b64_tr_b16 v[204:205], v178 offset:0x2080
	ds_read_b64_tr_b16 v[206:207], v178 offset:0x2280
	ds_read_b64_tr_b16 v[208:209], v179 offset:0x28a0
	ds_read_b64_tr_b16 v[210:211], v179 offset:0x2aa0
	ds_read_b64_tr_b16 v[212:213], v178 offset:0x28a0
	ds_read_b64_tr_b16 v[214:215], v178 offset:0x2aa0
	ds_read_b64_tr_b16 v[216:217], v179 offset:0x30c0
	ds_read_b64_tr_b16 v[218:219], v179 offset:0x32c0
	ds_read_b64_tr_b16 v[220:221], v178 offset:0x30c0
	ds_read_b64_tr_b16 v[222:223], v178 offset:0x32c0
	s_waitcnt lgkmcnt(4)
	s_nop 0
	v_mfma_f32_16x16x32_bf16 v[84:87], v[180:183], v[64:67], v[84:87]
	v_mfma_f32_16x16x32_bf16 v[92:95], v[180:183], v[68:71], v[92:95]
	v_mfma_f32_16x16x32_bf16 v[88:91], v[208:211], v[64:67], v[88:91]
	v_mfma_f32_16x16x32_bf16 v[96:99], v[208:211], v[68:71], v[96:99]
	v_mfma_f32_16x16x32_bf16 v[84:87], v[204:207], v[148:151], v[84:87]
	v_mfma_f32_16x16x32_bf16 v[92:95], v[204:207], v[152:155], v[92:95]
	v_mfma_f32_16x16x32_bf16 v[88:91], v[212:215], v[148:151], v[88:91]
	v_mfma_f32_16x16x32_bf16 v[96:99], v[212:215], v[152:155], v[96:99]
	ds_read_b64_tr_b16 v[180:181], v179 offset:0x38e0
	ds_read_b64_tr_b16 v[182:183], v179 offset:0x3ae0
	ds_read_b64_tr_b16 v[204:205], v178 offset:0x38e0
	ds_read_b64_tr_b16 v[206:207], v178 offset:0x3ae0
	s_waitcnt lgkmcnt(4)
	v_mfma_f32_16x16x32_bf16 v[60:63], v[216:219], v[64:67], v[60:63]
	s_waitcnt lgkmcnt(0)
	v_mfma_f32_16x16x32_bf16 v[80:83], v[216:219], v[68:71], v[80:83]
	v_mfma_f32_16x16x32_bf16 v[60:63], v[220:223], v[148:151], v[60:63]
	v_mfma_f32_16x16x32_bf16 v[80:83], v[220:223], v[152:155], v[80:83]
	v_mfma_f32_16x16x32_bf16 v[64:67], v[180:183], v[64:67], v[72:75]
	v_mfma_f32_16x16x32_bf16 v[68:71], v[180:183], v[68:71], v[76:79]
	v_mfma_f32_16x16x32_bf16 v[72:75], v[204:207], v[148:151], v[64:67]
	v_mfma_f32_16x16x32_bf16 v[76:79], v[204:207], v[152:155], v[68:71]
	s_nop 4
	v_fmamk_f32 v64, v144, 0x3e0293ee, v200
	v_exp_f32_e32 v144, v64
	v_fmamk_f32 v64, v145, 0x3e0293ee, v200
	v_exp_f32_e32 v148, v64
	v_fmamk_f32 v64, v146, 0x3e0293ee, v200
	v_exp_f32_e32 v146, v64
	v_fmamk_f32 v64, v147, 0x3e0293ee, v200
	v_exp_f32_e32 v150, v64
	v_fmamk_f32 v64, v140, 0x3e0293ee, v200
	v_exp_f32_e32 v145, v64
	v_fmamk_f32 v64, v141, 0x3e0293ee, v200
	v_exp_f32_e32 v149, v64
	v_fmamk_f32 v64, v142, 0x3e0293ee, v200
	v_exp_f32_e32 v147, v64
	v_fmamk_f32 v64, v143, 0x3e0293ee, v200
	v_exp_f32_e32 v151, v64
	v_fmamk_f32 v64, v136, 0x3e0293ee, v200
	v_exp_f32_e32 v136, v64
	v_fmamk_f32 v64, v137, 0x3e0293ee, v200
	v_exp_f32_e32 v140, v64
	v_fmamk_f32 v64, v138, 0x3e0293ee, v200
	v_exp_f32_e32 v138, v64
	v_fmamk_f32 v64, v139, 0x3e0293ee, v200
	v_exp_f32_e32 v142, v64
	v_fmamk_f32 v64, v132, 0x3e0293ee, v200
	v_exp_f32_e32 v137, v64
	v_fmamk_f32 v64, v133, 0x3e0293ee, v200
	v_exp_f32_e32 v141, v64
	v_fmamk_f32 v64, v134, 0x3e0293ee, v200
	v_exp_f32_e32 v139, v64
	v_fmamk_f32 v64, v135, 0x3e0293ee, v200
	v_exp_f32_e32 v143, v64
	s_and_b32 s22, s56, 0x4000
	v_add_u32_e32 v132, s22, v190
	v_cvt_pk_bf16_f32 v64, v144, v148
	v_cvt_pk_bf16_f32 v65, v146, v150
	v_cvt_pk_bf16_f32 v66, v136, v140
	v_cvt_pk_bf16_f32 v67, v138, v142
	v_cvt_pk_bf16_f32 v68, v145, v149
	v_cvt_pk_bf16_f32 v69, v147, v151
	v_cvt_pk_bf16_f32 v70, v137, v141
	v_cvt_pk_bf16_f32 v71, v139, v143
	ds_write_b128 v132, v[64:67]
	ds_write_b128 v132, v[68:71] offset:1024
	v_pk_add_f32 v[132:133], v[144:145], v[148:149]
	v_pk_add_f32 v[134:135], v[146:147], v[150:151]
	s_add_u32 s6, s6, 0xc0000
	v_pk_add_f32 v[132:133], v[132:133], v[134:135]
	v_pk_add_f32 v[134:135], v[136:137], v[140:141]
	v_pk_add_f32 v[136:137], v[138:139], v[142:143]
	s_addc_u32 s7, s7, 0
	v_pk_add_f32 v[134:135], v[134:135], v[136:137]
	s_add_i32 s55, s55, 1
	v_pk_add_f32 v[132:133], v[132:133], v[134:135]
	s_addk_i32 s56, 0x4000
	s_cmp_eq_u32 s6, 0xc240000
	v_pk_add_f32 v[174:175], v[174:175], v[132:133]
	s_cbranch_scc0 .LBB0_1271
; #define SBAR() __builtin_amdgcn_sched_barrier(0)
; #define ELOADV(kt) do { const char* vb_ = (const char*)Vh + (size_t)(kt) * (64 * LDV * 2); sv0 = *(const bf16x8*)(vb_ + voff0); sv1 = *(const bf16x8*)(vb_ + voff1); sv2 = *(const bf16x8*)(vb_ + voff0 + 256); sv3 = *(const bf16x8*)(vb_ + voff1 + 256); } while (0)
; #define ELOADK(kt) do { const char* kb_ = (const char*)Kh + (size_t)(kt) * (64 * LDK * 2); sk0 = *(const bf16x8*)(kb_ + koff0); sk1 = *(const bf16x8*)(kb_ + koff1); } while (0)
; #define EWRITEV(b) do { char* d_ = V_lds + (b) * D16_V; *(bf16x8*)(d_ + vst0) = sv0; *(bf16x8*)(d_ + vst1) = sv1; *(bf16x8*)(d_ + 8 * VP16 + vst0) = sv2; *(bf16x8*)(d_ + 8 * VP16 + vst1) = sv3; } while (0)
; #define EWRITEK(b) do { char* d_ = K_lds + (b) * PB_K; *(bf16x8*)(d_ + KSWZ(sr, sc * 2)) = sk0; *(bf16x8*)(d_ + KSWZ(32 + sr, sc * 2)) = sk1; } while (0)
; template <int LDQ, int LDK, int LDV, int LDO, int DMX> ...
;     ...
;   for (int t = 0; t < NT; ++t) {
;     __syncthreads();
;     bf16x8 pp[2]; { const char* d_ = P_oth + (t & 1) * (4 * PB_P); pp[0] = *(const bf16x8*)(d_); pp[1] = *(const bf16x8*)(d_ + 1024); }
;     const bf16x8 pc[2] = {po[0], po[1]};
;     const bool more = t + 1 < NT;
;     if (more) EQK((t + 1) & 1);
;     const int vb = vlane + (t & 1) * (int)D16_V, vbo = vb + ch * 1024, vbp = vb + (1 - ch) * 1024;
;     SBAR(); pv16d<0>(o, vbo, vbp, pc, pp); SBAR();
;     asm volatile("s_waitcnt vmcnt(0)" ::: "memory");
;     if (t + 2 < NT) EWRITEK(t & 1);
;     if (t + 1 < NT) EWRITEV((t + 1) & 1);
;     ELOADK(t + 3); ELOADV(t + 2);
;     SBAR(); pv16d<4>(o, vbo, vbp, pc, pp); SBAR();
;     if (more) ESM((t + 1) & 1);
;   }
;   __builtin_amdgcn_s_setprio(0);
;   ls0 += __shfl_xor(ls0, 16); ls0 += __shfl_xor(ls0, 32); ls1 += __shfl_xor(ls1, 16); ls1 += __shfl_xor(ls1, 32);
;   __syncthreads();
;   int l16e = l16, ge = g, wide = wid; asm volatile("" : "+v"(l16e), "+v"(ge), "+v"(wide));
;   const int rbe = wide & 3, che = wide >> 2;
;   if (ge == 0) { L_lds[wide * 32 + l16e] = ls0; L_lds[wide * 32 + 16 + l16e] = ls1; }
;   __syncthreads();
.LBB0_1273:
	s_waitcnt vmcnt(2) lgkmcnt(0)
	s_barrier
	ds_read_b128 v[32:35], v191 offset:16384
	ds_read_b128 v[132:135], v191 offset:17408
	ds_read_b64_tr_b16 v[4:5], v197 offset:0
	ds_read_b64_tr_b16 v[6:7], v197 offset:0x200
	ds_read_b64_tr_b16 v[8:9], v199 offset:0
	ds_read_b64_tr_b16 v[10:11], v199 offset:0x200
	ds_read_b64_tr_b16 v[12:13], v197 offset:0x820
	ds_read_b64_tr_b16 v[14:15], v197 offset:0xa20
	ds_read_b64_tr_b16 v[16:17], v199 offset:0x820
	ds_read_b64_tr_b16 v[18:19], v199 offset:0xa20
	ds_read_b64_tr_b16 v[20:21], v197 offset:0x1040
	ds_read_b64_tr_b16 v[22:23], v197 offset:0x1240
	ds_read_b64_tr_b16 v[24:25], v199 offset:0x1040
	ds_read_b64_tr_b16 v[26:27], v199 offset:0x1240
	s_waitcnt lgkmcnt(4)
	s_nop 0
	v_mfma_f32_16x16x32_bf16 v[28:31], v[4:7], v[64:67], v[128:131]
	v_mfma_f32_16x16x32_bf16 v[4:7], v[4:7], v[68:71], v[124:127]
	s_waitcnt vmcnt(3)
	v_mfma_f32_16x16x32_bf16 v[36:39], v[12:15], v[64:67], v[120:123]
	v_mfma_f32_16x16x32_bf16 v[12:15], v[12:15], v[68:71], v[112:115]
	s_waitcnt vmcnt(2) lgkmcnt(1)
	v_mfma_f32_16x16x32_bf16 v[40:43], v[8:11], v[32:35], v[28:31]
	s_waitcnt lgkmcnt(0)
	v_mfma_f32_16x16x32_bf16 v[8:11], v[8:11], v[132:135], v[4:7]
	v_mfma_f32_16x16x32_bf16 v[36:39], v[16:19], v[32:35], v[36:39]
	v_mfma_f32_16x16x32_bf16 v[4:7], v[16:19], v[132:135], v[12:15]
	ds_read_b64_tr_b16 v[16:17], v197 offset:0x1860
	ds_read_b64_tr_b16 v[18:19], v197 offset:0x1a60
	ds_read_b64_tr_b16 v[28:29], v199 offset:0x1860
	ds_read_b64_tr_b16 v[30:31], v199 offset:0x1a60
	s_waitcnt lgkmcnt(4)
	v_mfma_f32_16x16x32_bf16 v[12:15], v[20:23], v[64:67], v[108:111]
	s_waitcnt lgkmcnt(0)
	v_mfma_f32_16x16x32_bf16 v[20:23], v[20:23], v[68:71], v[116:119]
	s_waitcnt vmcnt(1)
	v_mfma_f32_16x16x32_bf16 v[44:47], v[24:27], v[32:35], v[12:15]
	v_mfma_f32_16x16x32_bf16 v[12:15], v[24:27], v[132:135], v[20:23]
	v_mfma_f32_16x16x32_bf16 v[20:23], v[16:19], v[64:67], v[100:103]
	v_mfma_f32_16x16x32_bf16 v[16:19], v[16:19], v[68:71], v[104:107]
	s_waitcnt vmcnt(0)
	v_mfma_f32_16x16x32_bf16 v[48:51], v[28:31], v[32:35], v[20:23]
	v_mfma_f32_16x16x32_bf16 v[16:19], v[28:31], v[132:135], v[16:19]
	s_waitcnt vmcnt(0)
	ds_read_b64_tr_b16 v[20:21], v197 offset:0x2080
	ds_read_b64_tr_b16 v[22:23], v197 offset:0x2280
	ds_read_b64_tr_b16 v[24:25], v199 offset:0x2080
	ds_read_b64_tr_b16 v[26:27], v199 offset:0x2280
	ds_read_b64_tr_b16 v[28:29], v197 offset:0x28a0
	ds_read_b64_tr_b16 v[30:31], v197 offset:0x2aa0
	ds_read_b64_tr_b16 v[100:101], v199 offset:0x28a0
	ds_read_b64_tr_b16 v[102:103], v199 offset:0x2aa0
	ds_read_b64_tr_b16 v[104:105], v197 offset:0x30c0
	ds_read_b64_tr_b16 v[106:107], v197 offset:0x32c0
	ds_read_b64_tr_b16 v[108:109], v199 offset:0x30c0
	ds_read_b64_tr_b16 v[110:111], v199 offset:0x32c0
	s_waitcnt lgkmcnt(4)
	s_nop 3
	v_mfma_f32_16x16x32_bf16 v[52:55], v[20:23], v[64:67], v[84:87]
	v_mfma_f32_16x16x32_bf16 v[20:23], v[20:23], v[68:71], v[92:95]
	v_mfma_f32_16x16x32_bf16 v[84:87], v[28:31], v[64:67], v[88:91]
	v_mfma_f32_16x16x32_bf16 v[28:31], v[28:31], v[68:71], v[96:99]
	v_mfma_f32_16x16x32_bf16 v[56:59], v[24:27], v[32:35], v[52:55]
	v_mfma_f32_16x16x32_bf16 v[24:27], v[24:27], v[132:135], v[20:23]
	v_mfma_f32_16x16x32_bf16 v[52:55], v[100:103], v[32:35], v[84:87]
	v_mfma_f32_16x16x32_bf16 v[20:23], v[100:103], v[132:135], v[28:31]
	ds_read_b64_tr_b16 v[84:85], v197 offset:0x38e0
	ds_read_b64_tr_b16 v[86:87], v197 offset:0x3ae0
	ds_read_b64_tr_b16 v[88:89], v199 offset:0x38e0
	ds_read_b64_tr_b16 v[90:91], v199 offset:0x3ae0
	s_waitcnt lgkmcnt(4)
	v_mfma_f32_16x16x32_bf16 v[28:31], v[104:107], v[64:67], v[60:63]
	s_waitcnt lgkmcnt(0)
	v_mfma_f32_16x16x32_bf16 v[80:83], v[104:107], v[68:71], v[80:83]
	v_mfma_f32_16x16x32_bf16 v[60:63], v[108:111], v[32:35], v[28:31]
	v_mfma_f32_16x16x32_bf16 v[28:31], v[108:111], v[132:135], v[80:83]
	v_mfma_f32_16x16x32_bf16 v[64:67], v[84:87], v[64:67], v[72:75]
	v_mfma_f32_16x16x32_bf16 v[68:71], v[84:87], v[68:71], v[76:79]
	v_mfma_f32_16x16x32_bf16 v[64:67], v[88:91], v[32:35], v[64:67]
	v_mfma_f32_16x16x32_bf16 v[32:35], v[88:91], v[132:135], v[68:71]
	s_setprio 0
	s_nop 4
	ds_bpermute_b32 v68, v185, v174
	ds_bpermute_b32 v69, v185, v175
	v_mov_b32_e32 v74, v187
	s_waitcnt lgkmcnt(0)
	s_barrier
	v_add_f32_e32 v71, v174, v68
	v_add_f32_e32 v70, v175, v69
	ds_bpermute_b32 v73, v186, v71
	ds_bpermute_b32 v72, v186, v70
	v_mov_b32_e32 v68, v189
	v_mov_b32_e32 v69, v188
	s_waitcnt lgkmcnt(0)
	s_nop 0
	v_cmp_eq_u32_e64 s[6:7], 0, v68
	v_cmp_ne_u32_e32 vcc, 0, v68
	v_lshlrev_b32_e32 v92, 5, v74
	s_and_saveexec_b64 s[22:23], vcc
	s_xor_b64 s[22:23], exec, s[22:23]
	v_lshlrev_b32_e32 v92, 5, v74
	s_or_saveexec_b64 s[22:23], s[22:23]
	v_lshlrev_b32_e32 v90, 2, v69
	s_xor_b64 exec, exec, s[22:23]
	v_add_f32_e32 v70, v70, v72
	v_lshlrev_b32_e32 v72, 7, v74
	v_add_f32_e32 v71, v71, v73
	v_add3_u32 v72, s45, v72, v90
	ds_write2_b32 v72, v71, v70 offset1:16
	s_or_b64 exec, exec, s[22:23]
	v_and_b32_e32 v72, 0x60, v92
	v_lshlrev_b32_e32 v91, 2, v72
	v_add3_u32 v73, s45, v90, v91
	s_waitcnt lgkmcnt(0)
	s_barrier
; template <int LDQ, int LDK, int LDV, int LDO, int DMX> ...
;     ...
;   float rl[2];
; #pragma unroll
;   for (int qt = 0; qt < 2; ++qt) rl[qt] = __builtin_amdgcn_rcpf(L_lds[rbe * 32 + 16 * qt + l16e] + L_lds[(rbe + 4) * 32 + 16 * qt + l16e]);
;   float* rowp = Ob + (long)(rbe * QBLK + l16e) * LDO + che * 128 + 4 * ge;
;   if (pass == 0) {
; #pragma unroll
;     for (int qt = 0; qt < 2; ++qt) { float* pq = rowp + (long)qt * 16 * LDO; asm volatile("" : "+v"(pq));
; #pragma unroll
;       for (int dt = 0; dt < 8; ++dt) *reinterpret_cast<f32x4a*>(pq + dt * 16) = o[dt][qt] * rl[qt]; }
;   } else {
;     float ssq[2];
; #pragma unroll
;     for (int qt = 0; qt < 2; ++qt) { const float* pq = rowp + (long)qt * 16 * LDO; asm volatile("" : "+v"(pq)); float q_ = 0.f;
; #pragma unroll
;       for (int dt = 0; dt < 8; ++dt) { const f32x4a v = *reinterpret_cast<const f32x4a*>(pq + dt * 16) - lam * (o[dt][qt] * rl[qt]); o[dt][qt] = v; q_ += (v[0] * v[0] + v[1] * v[1]) + (v[2] * v[2] + v[3] * v[3]); }
	ds_read2_b32 v[70:71], v73 offset1:16
	v_add3_u32 v74, s45, v91, v90
	ds_read_b32 v74, v74 offset:512
	ds_read_b32 v73, v73 offset:576
	v_add_u32_e32 v80, v72, v69
	v_ashrrev_i32_e32 v81, 31, v80
	v_and_b32_e32 v82, 0xffffff80, v92
	s_waitcnt lgkmcnt(1)
	v_add_f32_e32 v70, v70, v74
	v_rcp_f32_e32 v112, v70
	s_waitcnt lgkmcnt(0)
	v_add_f32_e32 v70, v71, v73
	v_rcp_f32_e32 v108, v70
	v_lshlrev_b64 v[70:71], 14, v[80:81]
	v_lshl_add_u64 v[70:71], s[16:17], 0, v[70:71]
	v_ashrrev_i32_e32 v83, 31, v82
	v_lshlrev_b32_e32 v84, 2, v68
	v_lshl_add_u64 v[70:71], v[82:83], 2, v[70:71]
	v_ashrrev_i32_e32 v85, 31, v84
	v_lshl_add_u64 v[114:115], v[84:85], 2, v[70:71]
	v_mov_b32_e32 v113, v112
	s_mov_b64 s[22:23], -1
	s_and_b64 vcc, exec, s[20:21]
	v_lshl_add_u64 v[110:111], v[114:115], 0, s[12:13]
	v_pk_mul_f32 v[74:75], v[40:41], v[112:113]
	v_pk_mul_f32 v[72:73], v[36:37], v[112:113]
	v_pk_mul_f32 v[70:71], v[44:45], v[112:113]
	v_pk_mul_f32 v[68:69], v[48:49], v[112:113]
	v_pk_mul_f32 v[48:49], v[56:57], v[112:113]
	v_pk_mul_f32 v[44:45], v[52:53], v[112:113]
	v_pk_mul_f32 v[40:41], v[60:61], v[112:113]
	v_pk_mul_f32 v[36:37], v[64:65], v[112:113]
	s_cbranch_vccz .LBB0_1281
	v_mov_b64_e32 v[52:53], v[114:115]
	flat_load_dwordx4 v[76:79], v[52:53]
	flat_load_dwordx4 v[94:97], v[52:53] offset:64
	flat_load_dwordx4 v[98:101], v[52:53] offset:128
	flat_load_dwordx4 v[116:119], v[52:53] offset:192
	flat_load_dwordx4 v[120:123], v[52:53] offset:256
	flat_load_dwordx4 v[124:127], v[52:53] offset:320
	flat_load_dwordx4 v[128:131], v[52:53] offset:384
	flat_load_dwordx4 v[132:135], v[52:53] offset:448
	v_mov_b64_e32 v[56:57], v[110:111]
	flat_load_dwordx4 v[174:177], v[56:57]
	flat_load_dwordx4 v[204:207], v[56:57] offset:64
	flat_load_dwordx4 v[208:211], v[56:57] offset:128
	flat_load_dwordx4 v[212:215], v[56:57] offset:192
	flat_load_dwordx4 v[216:219], v[56:57] offset:256
	flat_load_dwordx4 v[220:223], v[56:57] offset:320
	flat_load_dwordx4 v[224:227], v[56:57] offset:384
	flat_load_dwordx4 v[228:231], v[56:57] offset:448
	v_mov_b32_e32 v113, v112
	v_xor_b32_e32 v53, 0x80000000, v3
	v_xor_b32_e32 v52, 0x80000000, v2
	v_pk_mul_f32 v[60:61], v[42:43], v[112:113]
	v_pk_mul_f32 v[64:65], v[38:39], v[112:113]
	v_pk_mul_f32 v[102:103], v[46:47], v[112:113]
	v_pk_mul_f32 v[104:105], v[50:51], v[112:113]
	v_pk_mul_f32 v[136:137], v[58:59], v[112:113]
	v_pk_mul_f32 v[138:139], v[54:55], v[112:113]
	v_pk_mul_f32 v[140:141], v[62:63], v[112:113]
	v_pk_mul_f32 v[142:143], v[66:67], v[112:113]
	s_waitcnt vmcnt(0) lgkmcnt(0)
; template <int LDQ, int LDK, int LDV, int LDO, int DMX> ...
;     ...
;     for (int qt = 0; qt < 2; ++qt) { const float* pq = rowp + (long)qt * 16 * LDO; asm volatile("" : "+v"(pq)); float q_ = 0.f;
; #pragma unroll
;       for (int dt = 0; dt < 8; ++dt) { const f32x4a v = *reinterpret_cast<const f32x4a*>(pq + dt * 16) - lam * (o[dt][qt] * rl[qt]); o[dt][qt] = v; q_ += (v[0] * v[0] + v[1] * v[1]) + (v[2] * v[2] + v[3] * v[3]); }
;       q_ += __shfl_xor(q_, 16); q_ += __shfl_xor(q_, 32); ssq[qt] = q_; }
;     if (ge == 0) { S_lds[wide * 32 + l16e] = ssq[0]; S_lds[wide * 32 + 16 + l16e] = ssq[1]; }
	v_pk_fma_f32 v[180:181], v[52:53], v[60:61], v[78:79]
	v_pk_fma_f32 v[86:87], v[160:161], v[74:75], v[76:77] neg_lo:[1,0,0] neg_hi:[1,0,0]
	v_pk_fma_f32 v[178:179], v[52:53], v[64:65], v[96:97]
	v_pk_fma_f32 v[88:89], v[160:161], v[72:73], v[94:95] neg_lo:[1,0,0] neg_hi:[1,0,0]
	v_pk_fma_f32 v[100:101], v[52:53], v[102:103], v[100:101]
	v_pk_fma_f32 v[102:103], v[160:161], v[70:71], v[98:99] neg_lo:[1,0,0] neg_hi:[1,0,0]
	v_mul_f32_e32 v56, v87, v87
	v_mul_f32_e32 v57, v181, v181
	v_mul_f32_e32 v60, v89, v89
	v_mul_f32_e32 v61, v179, v179
	v_pk_fma_f32 v[104:105], v[52:53], v[104:105], v[118:119]
	v_pk_fma_f32 v[106:107], v[160:161], v[68:69], v[116:117] neg_lo:[1,0,0] neg_hi:[1,0,0]
	v_mul_f32_e32 v64, v103, v103
	v_mul_f32_e32 v65, v101, v101
	v_fmac_f32_e32 v56, v86, v86
	v_fmac_f32_e32 v57, v180, v180
	v_fmac_f32_e32 v60, v88, v88
	v_fmac_f32_e32 v61, v178, v178
	v_pk_fma_f32 v[152:153], v[52:53], v[136:137], v[122:123]
	v_pk_fma_f32 v[154:155], v[160:161], v[48:49], v[120:121] neg_lo:[1,0,0] neg_hi:[1,0,0]
	v_mul_f32_e32 v76, v107, v107
	v_mul_f32_e32 v77, v105, v105
	v_fmac_f32_e32 v64, v102, v102
	v_fmac_f32_e32 v65, v100, v100
	v_add_f32_e32 v56, v56, v57
	v_add_f32_e32 v57, v60, v61
	v_pk_fma_f32 v[148:149], v[52:53], v[138:139], v[126:127]
	v_pk_fma_f32 v[150:151], v[160:161], v[44:45], v[124:125] neg_lo:[1,0,0] neg_hi:[1,0,0]
	v_mul_f32_e32 v78, v155, v155
	v_mul_f32_e32 v79, v153, v153
	v_fmac_f32_e32 v76, v106, v106
	v_fmac_f32_e32 v77, v104, v104
	v_add_f32_e32 v60, v64, v65
	v_add_f32_e32 v56, v56, v57
	v_pk_fma_f32 v[144:145], v[52:53], v[140:141], v[130:131]
	v_pk_fma_f32 v[146:147], v[160:161], v[40:41], v[128:129] neg_lo:[1,0,0] neg_hi:[1,0,0]
	v_mul_f32_e32 v93, v151, v151
	v_mul_f32_e32 v94, v149, v149
	v_fmac_f32_e32 v78, v154, v154
	v_fmac_f32_e32 v79, v152, v152
	v_add_f32_e32 v61, v76, v77
	v_add_f32_e32 v56, v56, v60
	v_pk_fma_f32 v[140:141], v[52:53], v[142:143], v[134:135]
	v_pk_fma_f32 v[142:143], v[160:161], v[36:37], v[132:133] neg_lo:[1,0,0] neg_hi:[1,0,0]
	v_mul_f32_e32 v95, v147, v147
	v_mul_f32_e32 v96, v145, v145
	v_fmac_f32_e32 v93, v150, v150
	v_fmac_f32_e32 v94, v148, v148
	v_add_f32_e32 v64, v78, v79
	v_add_f32_e32 v56, v56, v61
	v_mul_f32_e32 v97, v143, v143
	v_mul_f32_e32 v98, v141, v141
	v_fmac_f32_e32 v95, v146, v146
	v_fmac_f32_e32 v96, v144, v144
	v_add_f32_e32 v65, v93, v94
	v_add_f32_e32 v56, v56, v64
	v_fmac_f32_e32 v97, v142, v142
	v_fmac_f32_e32 v98, v140, v140
	v_add_f32_e32 v76, v95, v96
	v_add_f32_e32 v56, v56, v65
	v_add_f32_e32 v56, v56, v76
	v_add_f32_e32 v57, v97, v98
	v_add_f32_e32 v78, v56, v57
	v_pk_mul_f32 v[56:57], v[10:11], v[108:109] op_sel_hi:[1,0]
	v_pk_mul_f32 v[60:61], v[8:9], v[108:109] op_sel_hi:[1,0]
	v_pk_fma_f32 v[136:137], v[52:53], v[56:57], v[176:177]
	v_pk_fma_f32 v[138:139], v[160:161], v[60:61], v[174:175] neg_lo:[1,0,0] neg_hi:[1,0,0]
	v_mul_f32_e32 v57, v137, v137
	v_mul_f32_e32 v56, v139, v139
	v_fmac_f32_e32 v56, v138, v138
	v_fmac_f32_e32 v57, v136, v136
	v_add_f32_e32 v64, v56, v57
	v_pk_mul_f32 v[56:57], v[6:7], v[108:109] op_sel_hi:[1,0]
	v_pk_mul_f32 v[60:61], v[4:5], v[108:109] op_sel_hi:[1,0]
	v_pk_fma_f32 v[132:133], v[52:53], v[56:57], v[206:207]
	v_pk_fma_f32 v[134:135], v[160:161], v[60:61], v[204:205] neg_lo:[1,0,0] neg_hi:[1,0,0]
	v_mul_f32_e32 v57, v133, v133
	v_mul_f32_e32 v56, v135, v135
	v_fmac_f32_e32 v56, v134, v134
	v_fmac_f32_e32 v57, v132, v132
	v_add_f32_e32 v56, v56, v57
	v_add_f32_e32 v64, v64, v56
	v_pk_mul_f32 v[56:57], v[14:15], v[108:109] op_sel_hi:[1,0]
	v_pk_mul_f32 v[60:61], v[12:13], v[108:109] op_sel_hi:[1,0]
	v_pk_fma_f32 v[128:129], v[52:53], v[56:57], v[210:211]
	v_pk_fma_f32 v[130:131], v[160:161], v[60:61], v[208:209] neg_lo:[1,0,0] neg_hi:[1,0,0]
	v_mul_f32_e32 v57, v129, v129
	v_mul_f32_e32 v56, v131, v131
	v_fmac_f32_e32 v56, v130, v130
	v_fmac_f32_e32 v57, v128, v128
	v_add_f32_e32 v56, v56, v57
	v_add_f32_e32 v64, v64, v56
	v_pk_mul_f32 v[56:57], v[18:19], v[108:109] op_sel_hi:[1,0]
	v_pk_mul_f32 v[60:61], v[16:17], v[108:109] op_sel_hi:[1,0]
	v_pk_fma_f32 v[124:125], v[52:53], v[56:57], v[214:215]
	v_pk_fma_f32 v[126:127], v[160:161], v[60:61], v[212:213] neg_lo:[1,0,0] neg_hi:[1,0,0]
	v_mul_f32_e32 v57, v125, v125
	v_mul_f32_e32 v56, v127, v127
	v_fmac_f32_e32 v56, v126, v126
	v_fmac_f32_e32 v57, v124, v124
	v_add_f32_e32 v56, v56, v57
	v_add_f32_e32 v64, v64, v56
	v_pk_mul_f32 v[56:57], v[26:27], v[108:109] op_sel_hi:[1,0]
	v_pk_mul_f32 v[60:61], v[24:25], v[108:109] op_sel_hi:[1,0]
	v_pk_fma_f32 v[120:121], v[52:53], v[56:57], v[218:219]
	v_pk_fma_f32 v[122:123], v[160:161], v[60:61], v[216:217] neg_lo:[1,0,0] neg_hi:[1,0,0]
	v_mul_f32_e32 v57, v121, v121
	v_mul_f32_e32 v56, v123, v123
	v_fmac_f32_e32 v56, v122, v122
	v_fmac_f32_e32 v57, v120, v120
	v_add_f32_e32 v56, v56, v57
	v_add_f32_e32 v64, v64, v56
	v_pk_mul_f32 v[56:57], v[22:23], v[108:109] op_sel_hi:[1,0]
	v_pk_mul_f32 v[60:61], v[20:21], v[108:109] op_sel_hi:[1,0]
	v_pk_fma_f32 v[116:117], v[52:53], v[56:57], v[222:223]
	v_pk_fma_f32 v[118:119], v[160:161], v[60:61], v[220:221] neg_lo:[1,0,0] neg_hi:[1,0,0]
	v_mul_f32_e32 v57, v117, v117
	v_mul_f32_e32 v56, v119, v119
	v_fmac_f32_e32 v56, v118, v118
	v_fmac_f32_e32 v57, v116, v116
	v_add_f32_e32 v56, v56, v57
	v_add_f32_e32 v76, v64, v56
	v_pk_mul_f32 v[56:57], v[30:31], v[108:109] op_sel_hi:[1,0]
	v_pk_mul_f32 v[64:65], v[28:29], v[108:109] op_sel_hi:[1,0]
	v_pk_fma_f32 v[60:61], v[52:53], v[56:57], v[226:227]
	v_pk_fma_f32 v[64:65], v[160:161], v[64:65], v[224:225] neg_lo:[1,0,0] neg_hi:[1,0,0]
	v_mul_f32_e32 v57, v61, v61
	v_mul_f32_e32 v56, v65, v65
	v_fmac_f32_e32 v56, v64, v64
	v_fmac_f32_e32 v57, v60, v60
	v_add_f32_e32 v56, v56, v57
	v_add_f32_e32 v93, v76, v56
	v_pk_mul_f32 v[56:57], v[34:35], v[108:109] op_sel_hi:[1,0]
	v_pk_mul_f32 v[76:77], v[32:33], v[108:109] op_sel_hi:[1,0]
	v_pk_fma_f32 v[52:53], v[52:53], v[56:57], v[230:231]
	v_pk_fma_f32 v[56:57], v[160:161], v[76:77], v[228:229] neg_lo:[1,0,0] neg_hi:[1,0,0]
	v_mul_f32_e32 v77, v53, v53
	v_mul_f32_e32 v76, v57, v57
	v_fmac_f32_e32 v76, v56, v56
	v_fmac_f32_e32 v77, v52, v52
	v_add_f32_e32 v76, v76, v77
	v_add_f32_e32 v93, v93, v76
	ds_bpermute_b32 v79, v185, v78
	ds_bpermute_b32 v94, v185, v93
	s_waitcnt lgkmcnt(1)
	v_add_f32_e32 v76, v78, v79
	s_waitcnt lgkmcnt(0)
	v_add_f32_e32 v78, v93, v94
	ds_bpermute_b32 v77, v186, v76
	ds_bpermute_b32 v79, v186, v78
	s_and_saveexec_b64 s[22:23], s[6:7]
	s_cbranch_execz .LBB0_1280
	v_lshlrev_b32_e32 v92, 2, v92
	v_add3_u32 v92, s46, v92, v90
	s_waitcnt lgkmcnt(1)
	v_add_f32_e32 v76, v76, v77
	s_waitcnt lgkmcnt(0)
	v_add_f32_e32 v77, v78, v79
	ds_write2_b32 v92, v76, v77 offset1:16
